# baseline (speedup 1.0000x reference)
_Z11prep_kernelPKfS0_S0_PDF16_PfPiS0_S1_:
	s_cmpk_lt_u32 s2, 0xc1
	s_mov_b64 s[4:5], -1
	s_cbranch_scc0 .LBB0_51
	s_cmpk_lg_i32 s2, 0xc0
	s_cbranch_scc0 .LBB0_11
	s_cmp_gt_u32 s2, 63
	s_cbranch_scc0 .LBB0_8
	s_load_dwordx4 s[4:7], s[0:1], 0x0
	s_load_dwordx2 s[28:29], s[0:1], 0x20
	s_sub_u32 s3, s2, 64
	v_readfirstlane_b32 s23, v0
	v_and_b32_e32 v1, 63, v0
	v_lshlrev_b32_e32 v100, 3, v1
	s_lshr_b32 s23, s23, 6
	s_lshr_b32 s27, s3, 2
	s_and_b32 s30, s3, 3
	s_lshl_b32 s8, s27, 13
	s_lshl_b32 s9, s23, 6
	s_add_u32 s8, s8, s9
	s_lshl_b32 s10, s23, 15
	s_lshl_b32 s9, s30, 9
	s_add_u32 s10, s10, s9
	s_waitcnt lgkmcnt(0)
	s_add_u32 s20, s4, s8
	s_addc_u32 s21, s5, 0
	s_add_u32 s24, s6, s10
	s_addc_u32 s25, s7, 0
	global_load_dwordx2 v[34:35], v100, s[24:25]
	global_load_dwordx2 v[36:37], v100, s[24:25] offset:2048
	s_add_u32 s24, s24, 0x1000
	s_addc_u32 s25, s25, 0
	s_load_dwordx8 s[32:39], s[20:21], 0x0
	s_load_dwordx8 s[40:47], s[20:21], 0x200
	s_load_dwordx8 s[48:55], s[20:21], 0x400
	s_load_dwordx8 s[56:63], s[20:21], 0x600
	global_load_dwordx2 v[38:39], v100, s[24:25]
	global_load_dwordx2 v[40:41], v100, s[24:25] offset:2048
	s_add_u32 s24, s24, 0x1000
	s_addc_u32 s25, s25, 0
	s_load_dwordx8 s[64:71], s[20:21], 0x20
	s_load_dwordx8 s[72:79], s[20:21], 0x220
	s_load_dwordx8 s[80:87], s[20:21], 0x420
	s_load_dwordx8 s[88:95], s[20:21], 0x620
	global_load_dwordx2 v[42:43], v100, s[24:25]
	global_load_dwordx2 v[44:45], v100, s[24:25] offset:2048
	s_add_u32 s24, s24, 0x1000
	s_addc_u32 s25, s25, 0
	global_load_dwordx2 v[46:47], v100, s[24:25]
	global_load_dwordx2 v[48:49], v100, s[24:25] offset:2048
	s_add_u32 s24, s24, 0x1000
	s_addc_u32 s25, s25, 0
	global_load_dwordx2 v[50:51], v100, s[24:25]
	global_load_dwordx2 v[52:53], v100, s[24:25] offset:2048
	s_add_u32 s24, s24, 0x1000
	s_addc_u32 s25, s25, 0
	global_load_dwordx2 v[54:55], v100, s[24:25]
	global_load_dwordx2 v[56:57], v100, s[24:25] offset:2048
	s_add_u32 s24, s24, 0x1000
	s_addc_u32 s25, s25, 0
	global_load_dwordx2 v[58:59], v100, s[24:25]
	global_load_dwordx2 v[60:61], v100, s[24:25] offset:2048
	s_add_u32 s24, s24, 0x1000
	s_addc_u32 s25, s25, 0
	global_load_dwordx2 v[62:63], v100, s[24:25]
	global_load_dwordx2 v[64:65], v100, s[24:25] offset:2048
	v_mov_b64_e32 v[2:3], 0
	v_mov_b64_e32 v[4:5], 0
	v_mov_b64_e32 v[6:7], 0
	v_mov_b64_e32 v[8:9], 0
	v_mov_b64_e32 v[10:11], 0
	v_mov_b64_e32 v[12:13], 0
	v_mov_b64_e32 v[14:15], 0
	v_mov_b64_e32 v[16:17], 0
	v_mov_b64_e32 v[18:19], 0
	v_mov_b64_e32 v[20:21], 0
	v_mov_b64_e32 v[22:23], 0
	v_mov_b64_e32 v[24:25], 0
	v_mov_b64_e32 v[26:27], 0
	v_mov_b64_e32 v[28:29], 0
	v_mov_b64_e32 v[30:31], 0
	v_mov_b64_e32 v[32:33], 0
	s_waitcnt lgkmcnt(0)
	s_waitcnt vmcnt(15)
	v_pk_fma_f32 v[2:3], s[32:33], v[34:35], v[2:3] op_sel_hi:[0,1,1]
	v_pk_fma_f32 v[4:5], s[40:41], v[34:35], v[4:5] op_sel_hi:[0,1,1]
	v_pk_fma_f32 v[6:7], s[48:49], v[34:35], v[6:7] op_sel_hi:[0,1,1]
	v_pk_fma_f32 v[8:9], s[56:57], v[34:35], v[8:9] op_sel_hi:[0,1,1]
	s_waitcnt vmcnt(14)
	v_pk_fma_f32 v[2:3], s[32:33], v[36:37], v[2:3] op_sel:[1,0,0]
	v_pk_fma_f32 v[4:5], s[40:41], v[36:37], v[4:5] op_sel:[1,0,0]
	v_pk_fma_f32 v[6:7], s[48:49], v[36:37], v[6:7] op_sel:[1,0,0]
	v_pk_fma_f32 v[8:9], s[56:57], v[36:37], v[8:9] op_sel:[1,0,0]
	s_waitcnt vmcnt(13)
	v_pk_fma_f32 v[2:3], s[34:35], v[38:39], v[2:3] op_sel_hi:[0,1,1]
	v_pk_fma_f32 v[4:5], s[42:43], v[38:39], v[4:5] op_sel_hi:[0,1,1]
	v_pk_fma_f32 v[6:7], s[50:51], v[38:39], v[6:7] op_sel_hi:[0,1,1]
	v_pk_fma_f32 v[8:9], s[58:59], v[38:39], v[8:9] op_sel_hi:[0,1,1]
	s_waitcnt vmcnt(12)
	v_pk_fma_f32 v[2:3], s[34:35], v[40:41], v[2:3] op_sel:[1,0,0]
	v_pk_fma_f32 v[4:5], s[42:43], v[40:41], v[4:5] op_sel:[1,0,0]
	v_pk_fma_f32 v[6:7], s[50:51], v[40:41], v[6:7] op_sel:[1,0,0]
	v_pk_fma_f32 v[8:9], s[58:59], v[40:41], v[8:9] op_sel:[1,0,0]
	s_waitcnt vmcnt(11)
	v_pk_fma_f32 v[2:3], s[36:37], v[42:43], v[2:3] op_sel_hi:[0,1,1]
	v_pk_fma_f32 v[4:5], s[44:45], v[42:43], v[4:5] op_sel_hi:[0,1,1]
	v_pk_fma_f32 v[6:7], s[52:53], v[42:43], v[6:7] op_sel_hi:[0,1,1]
	v_pk_fma_f32 v[8:9], s[60:61], v[42:43], v[8:9] op_sel_hi:[0,1,1]
	s_waitcnt vmcnt(10)
	v_pk_fma_f32 v[2:3], s[36:37], v[44:45], v[2:3] op_sel:[1,0,0]
	v_pk_fma_f32 v[4:5], s[44:45], v[44:45], v[4:5] op_sel:[1,0,0]
	v_pk_fma_f32 v[6:7], s[52:53], v[44:45], v[6:7] op_sel:[1,0,0]
	v_pk_fma_f32 v[8:9], s[60:61], v[44:45], v[8:9] op_sel:[1,0,0]
	s_waitcnt vmcnt(9)
	v_pk_fma_f32 v[2:3], s[38:39], v[46:47], v[2:3] op_sel_hi:[0,1,1]
	v_pk_fma_f32 v[4:5], s[46:47], v[46:47], v[4:5] op_sel_hi:[0,1,1]
	v_pk_fma_f32 v[6:7], s[54:55], v[46:47], v[6:7] op_sel_hi:[0,1,1]
	v_pk_fma_f32 v[8:9], s[62:63], v[46:47], v[8:9] op_sel_hi:[0,1,1]
	s_waitcnt vmcnt(8)
	v_pk_fma_f32 v[2:3], s[38:39], v[48:49], v[2:3] op_sel:[1,0,0]
	v_pk_fma_f32 v[4:5], s[46:47], v[48:49], v[4:5] op_sel:[1,0,0]
	v_pk_fma_f32 v[6:7], s[54:55], v[48:49], v[6:7] op_sel:[1,0,0]
	v_pk_fma_f32 v[8:9], s[62:63], v[48:49], v[8:9] op_sel:[1,0,0]
	s_load_dwordx8 s[32:39], s[20:21], 0x800
	s_load_dwordx8 s[40:47], s[20:21], 0xa00
	s_load_dwordx8 s[48:55], s[20:21], 0xc00
	s_load_dwordx8 s[56:63], s[20:21], 0xe00
	s_waitcnt vmcnt(7)
	v_pk_fma_f32 v[2:3], s[64:65], v[50:51], v[2:3] op_sel_hi:[0,1,1]
	v_pk_fma_f32 v[4:5], s[72:73], v[50:51], v[4:5] op_sel_hi:[0,1,1]
	v_pk_fma_f32 v[6:7], s[80:81], v[50:51], v[6:7] op_sel_hi:[0,1,1]
	v_pk_fma_f32 v[8:9], s[88:89], v[50:51], v[8:9] op_sel_hi:[0,1,1]
	s_waitcnt vmcnt(6)
	v_pk_fma_f32 v[2:3], s[64:65], v[52:53], v[2:3] op_sel:[1,0,0]
	v_pk_fma_f32 v[4:5], s[72:73], v[52:53], v[4:5] op_sel:[1,0,0]
	v_pk_fma_f32 v[6:7], s[80:81], v[52:53], v[6:7] op_sel:[1,0,0]
	v_pk_fma_f32 v[8:9], s[88:89], v[52:53], v[8:9] op_sel:[1,0,0]
	s_waitcnt vmcnt(5)
	v_pk_fma_f32 v[2:3], s[66:67], v[54:55], v[2:3] op_sel_hi:[0,1,1]
	v_pk_fma_f32 v[4:5], s[74:75], v[54:55], v[4:5] op_sel_hi:[0,1,1]
	v_pk_fma_f32 v[6:7], s[82:83], v[54:55], v[6:7] op_sel_hi:[0,1,1]
	v_pk_fma_f32 v[8:9], s[90:91], v[54:55], v[8:9] op_sel_hi:[0,1,1]
	s_waitcnt vmcnt(4)
	v_pk_fma_f32 v[2:3], s[66:67], v[56:57], v[2:3] op_sel:[1,0,0]
	v_pk_fma_f32 v[4:5], s[74:75], v[56:57], v[4:5] op_sel:[1,0,0]
	v_pk_fma_f32 v[6:7], s[82:83], v[56:57], v[6:7] op_sel:[1,0,0]
	v_pk_fma_f32 v[8:9], s[90:91], v[56:57], v[8:9] op_sel:[1,0,0]
	s_waitcnt vmcnt(3)
	v_pk_fma_f32 v[2:3], s[68:69], v[58:59], v[2:3] op_sel_hi:[0,1,1]
	v_pk_fma_f32 v[4:5], s[76:77], v[58:59], v[4:5] op_sel_hi:[0,1,1]
	v_pk_fma_f32 v[6:7], s[84:85], v[58:59], v[6:7] op_sel_hi:[0,1,1]
	v_pk_fma_f32 v[8:9], s[92:93], v[58:59], v[8:9] op_sel_hi:[0,1,1]
	s_waitcnt vmcnt(2)
	v_pk_fma_f32 v[2:3], s[68:69], v[60:61], v[2:3] op_sel:[1,0,0]
	v_pk_fma_f32 v[4:5], s[76:77], v[60:61], v[4:5] op_sel:[1,0,0]
	v_pk_fma_f32 v[6:7], s[84:85], v[60:61], v[6:7] op_sel:[1,0,0]
	v_pk_fma_f32 v[8:9], s[92:93], v[60:61], v[8:9] op_sel:[1,0,0]
	s_waitcnt vmcnt(1)
	v_pk_fma_f32 v[2:3], s[70:71], v[62:63], v[2:3] op_sel_hi:[0,1,1]
	v_pk_fma_f32 v[4:5], s[78:79], v[62:63], v[4:5] op_sel_hi:[0,1,1]
	v_pk_fma_f32 v[6:7], s[86:87], v[62:63], v[6:7] op_sel_hi:[0,1,1]
	v_pk_fma_f32 v[8:9], s[94:95], v[62:63], v[8:9] op_sel_hi:[0,1,1]
	s_waitcnt vmcnt(0)
	v_pk_fma_f32 v[2:3], s[70:71], v[64:65], v[2:3] op_sel:[1,0,0]
	v_pk_fma_f32 v[4:5], s[78:79], v[64:65], v[4:5] op_sel:[1,0,0]
	v_pk_fma_f32 v[6:7], s[86:87], v[64:65], v[6:7] op_sel:[1,0,0]
	v_pk_fma_f32 v[8:9], s[94:95], v[64:65], v[8:9] op_sel:[1,0,0]
	s_waitcnt lgkmcnt(0)
	s_load_dwordx8 s[64:71], s[20:21], 0x820
	s_load_dwordx8 s[72:79], s[20:21], 0xa20
	s_load_dwordx8 s[80:87], s[20:21], 0xc20
	s_load_dwordx8 s[88:95], s[20:21], 0xe20
	v_pk_fma_f32 v[10:11], s[32:33], v[34:35], v[10:11] op_sel_hi:[0,1,1]
	v_pk_fma_f32 v[12:13], s[40:41], v[34:35], v[12:13] op_sel_hi:[0,1,1]
	v_pk_fma_f32 v[14:15], s[48:49], v[34:35], v[14:15] op_sel_hi:[0,1,1]
	v_pk_fma_f32 v[16:17], s[56:57], v[34:35], v[16:17] op_sel_hi:[0,1,1]
	v_pk_fma_f32 v[10:11], s[32:33], v[36:37], v[10:11] op_sel:[1,0,0]
	v_pk_fma_f32 v[12:13], s[40:41], v[36:37], v[12:13] op_sel:[1,0,0]
	v_pk_fma_f32 v[14:15], s[48:49], v[36:37], v[14:15] op_sel:[1,0,0]
	v_pk_fma_f32 v[16:17], s[56:57], v[36:37], v[16:17] op_sel:[1,0,0]
	v_pk_fma_f32 v[10:11], s[34:35], v[38:39], v[10:11] op_sel_hi:[0,1,1]
	v_pk_fma_f32 v[12:13], s[42:43], v[38:39], v[12:13] op_sel_hi:[0,1,1]
	v_pk_fma_f32 v[14:15], s[50:51], v[38:39], v[14:15] op_sel_hi:[0,1,1]
	v_pk_fma_f32 v[16:17], s[58:59], v[38:39], v[16:17] op_sel_hi:[0,1,1]
	v_pk_fma_f32 v[10:11], s[34:35], v[40:41], v[10:11] op_sel:[1,0,0]
	v_pk_fma_f32 v[12:13], s[42:43], v[40:41], v[12:13] op_sel:[1,0,0]
	v_pk_fma_f32 v[14:15], s[50:51], v[40:41], v[14:15] op_sel:[1,0,0]
	v_pk_fma_f32 v[16:17], s[58:59], v[40:41], v[16:17] op_sel:[1,0,0]
	v_pk_fma_f32 v[10:11], s[36:37], v[42:43], v[10:11] op_sel_hi:[0,1,1]
	v_pk_fma_f32 v[12:13], s[44:45], v[42:43], v[12:13] op_sel_hi:[0,1,1]
	v_pk_fma_f32 v[14:15], s[52:53], v[42:43], v[14:15] op_sel_hi:[0,1,1]
	v_pk_fma_f32 v[16:17], s[60:61], v[42:43], v[16:17] op_sel_hi:[0,1,1]
	v_pk_fma_f32 v[10:11], s[36:37], v[44:45], v[10:11] op_sel:[1,0,0]
	v_pk_fma_f32 v[12:13], s[44:45], v[44:45], v[12:13] op_sel:[1,0,0]
	v_pk_fma_f32 v[14:15], s[52:53], v[44:45], v[14:15] op_sel:[1,0,0]
	v_pk_fma_f32 v[16:17], s[60:61], v[44:45], v[16:17] op_sel:[1,0,0]
	v_pk_fma_f32 v[10:11], s[38:39], v[46:47], v[10:11] op_sel_hi:[0,1,1]
	v_pk_fma_f32 v[12:13], s[46:47], v[46:47], v[12:13] op_sel_hi:[0,1,1]
	v_pk_fma_f32 v[14:15], s[54:55], v[46:47], v[14:15] op_sel_hi:[0,1,1]
	v_pk_fma_f32 v[16:17], s[62:63], v[46:47], v[16:17] op_sel_hi:[0,1,1]
	v_pk_fma_f32 v[10:11], s[38:39], v[48:49], v[10:11] op_sel:[1,0,0]
	v_pk_fma_f32 v[12:13], s[46:47], v[48:49], v[12:13] op_sel:[1,0,0]
	v_pk_fma_f32 v[14:15], s[54:55], v[48:49], v[14:15] op_sel:[1,0,0]
	v_pk_fma_f32 v[16:17], s[62:63], v[48:49], v[16:17] op_sel:[1,0,0]
	s_waitcnt lgkmcnt(0)
	s_load_dwordx8 s[32:39], s[20:21], 0x1000
	s_load_dwordx8 s[40:47], s[20:21], 0x1200
	s_load_dwordx8 s[48:55], s[20:21], 0x1400
	s_load_dwordx8 s[56:63], s[20:21], 0x1600
	v_pk_fma_f32 v[10:11], s[64:65], v[50:51], v[10:11] op_sel_hi:[0,1,1]
	v_pk_fma_f32 v[12:13], s[72:73], v[50:51], v[12:13] op_sel_hi:[0,1,1]
	v_pk_fma_f32 v[14:15], s[80:81], v[50:51], v[14:15] op_sel_hi:[0,1,1]
	v_pk_fma_f32 v[16:17], s[88:89], v[50:51], v[16:17] op_sel_hi:[0,1,1]
	v_pk_fma_f32 v[10:11], s[64:65], v[52:53], v[10:11] op_sel:[1,0,0]
	v_pk_fma_f32 v[12:13], s[72:73], v[52:53], v[12:13] op_sel:[1,0,0]
	v_pk_fma_f32 v[14:15], s[80:81], v[52:53], v[14:15] op_sel:[1,0,0]
	v_pk_fma_f32 v[16:17], s[88:89], v[52:53], v[16:17] op_sel:[1,0,0]
	v_pk_fma_f32 v[10:11], s[66:67], v[54:55], v[10:11] op_sel_hi:[0,1,1]
	v_pk_fma_f32 v[12:13], s[74:75], v[54:55], v[12:13] op_sel_hi:[0,1,1]
	v_pk_fma_f32 v[14:15], s[82:83], v[54:55], v[14:15] op_sel_hi:[0,1,1]
	v_pk_fma_f32 v[16:17], s[90:91], v[54:55], v[16:17] op_sel_hi:[0,1,1]
	v_pk_fma_f32 v[10:11], s[66:67], v[56:57], v[10:11] op_sel:[1,0,0]
	v_pk_fma_f32 v[12:13], s[74:75], v[56:57], v[12:13] op_sel:[1,0,0]
	v_pk_fma_f32 v[14:15], s[82:83], v[56:57], v[14:15] op_sel:[1,0,0]
	v_pk_fma_f32 v[16:17], s[90:91], v[56:57], v[16:17] op_sel:[1,0,0]
	v_pk_fma_f32 v[10:11], s[68:69], v[58:59], v[10:11] op_sel_hi:[0,1,1]
	v_pk_fma_f32 v[12:13], s[76:77], v[58:59], v[12:13] op_sel_hi:[0,1,1]
	v_pk_fma_f32 v[14:15], s[84:85], v[58:59], v[14:15] op_sel_hi:[0,1,1]
	v_pk_fma_f32 v[16:17], s[92:93], v[58:59], v[16:17] op_sel_hi:[0,1,1]
	v_pk_fma_f32 v[10:11], s[68:69], v[60:61], v[10:11] op_sel:[1,0,0]
	v_pk_fma_f32 v[12:13], s[76:77], v[60:61], v[12:13] op_sel:[1,0,0]
	v_pk_fma_f32 v[14:15], s[84:85], v[60:61], v[14:15] op_sel:[1,0,0]
	v_pk_fma_f32 v[16:17], s[92:93], v[60:61], v[16:17] op_sel:[1,0,0]
	v_pk_fma_f32 v[10:11], s[70:71], v[62:63], v[10:11] op_sel_hi:[0,1,1]
	v_pk_fma_f32 v[12:13], s[78:79], v[62:63], v[12:13] op_sel_hi:[0,1,1]
	v_pk_fma_f32 v[14:15], s[86:87], v[62:63], v[14:15] op_sel_hi:[0,1,1]
	v_pk_fma_f32 v[16:17], s[94:95], v[62:63], v[16:17] op_sel_hi:[0,1,1]
	v_pk_fma_f32 v[10:11], s[70:71], v[64:65], v[10:11] op_sel:[1,0,0]
	v_pk_fma_f32 v[12:13], s[78:79], v[64:65], v[12:13] op_sel:[1,0,0]
	v_pk_fma_f32 v[14:15], s[86:87], v[64:65], v[14:15] op_sel:[1,0,0]
	v_pk_fma_f32 v[16:17], s[94:95], v[64:65], v[16:17] op_sel:[1,0,0]
	s_waitcnt lgkmcnt(0)
	s_load_dwordx8 s[64:71], s[20:21], 0x1020
	s_load_dwordx8 s[72:79], s[20:21], 0x1220
	s_load_dwordx8 s[80:87], s[20:21], 0x1420
	s_load_dwordx8 s[88:95], s[20:21], 0x1620
	v_pk_fma_f32 v[18:19], s[32:33], v[34:35], v[18:19] op_sel_hi:[0,1,1]
	v_pk_fma_f32 v[20:21], s[40:41], v[34:35], v[20:21] op_sel_hi:[0,1,1]
	v_pk_fma_f32 v[22:23], s[48:49], v[34:35], v[22:23] op_sel_hi:[0,1,1]
	v_pk_fma_f32 v[24:25], s[56:57], v[34:35], v[24:25] op_sel_hi:[0,1,1]
	v_pk_fma_f32 v[18:19], s[32:33], v[36:37], v[18:19] op_sel:[1,0,0]
	v_pk_fma_f32 v[20:21], s[40:41], v[36:37], v[20:21] op_sel:[1,0,0]
	v_pk_fma_f32 v[22:23], s[48:49], v[36:37], v[22:23] op_sel:[1,0,0]
	v_pk_fma_f32 v[24:25], s[56:57], v[36:37], v[24:25] op_sel:[1,0,0]
	v_pk_fma_f32 v[18:19], s[34:35], v[38:39], v[18:19] op_sel_hi:[0,1,1]
	v_pk_fma_f32 v[20:21], s[42:43], v[38:39], v[20:21] op_sel_hi:[0,1,1]
	v_pk_fma_f32 v[22:23], s[50:51], v[38:39], v[22:23] op_sel_hi:[0,1,1]
	v_pk_fma_f32 v[24:25], s[58:59], v[38:39], v[24:25] op_sel_hi:[0,1,1]
	v_pk_fma_f32 v[18:19], s[34:35], v[40:41], v[18:19] op_sel:[1,0,0]
	v_pk_fma_f32 v[20:21], s[42:43], v[40:41], v[20:21] op_sel:[1,0,0]
	v_pk_fma_f32 v[22:23], s[50:51], v[40:41], v[22:23] op_sel:[1,0,0]
	v_pk_fma_f32 v[24:25], s[58:59], v[40:41], v[24:25] op_sel:[1,0,0]
	v_pk_fma_f32 v[18:19], s[36:37], v[42:43], v[18:19] op_sel_hi:[0,1,1]
	v_pk_fma_f32 v[20:21], s[44:45], v[42:43], v[20:21] op_sel_hi:[0,1,1]
	v_pk_fma_f32 v[22:23], s[52:53], v[42:43], v[22:23] op_sel_hi:[0,1,1]
	v_pk_fma_f32 v[24:25], s[60:61], v[42:43], v[24:25] op_sel_hi:[0,1,1]
	v_pk_fma_f32 v[18:19], s[36:37], v[44:45], v[18:19] op_sel:[1,0,0]
	v_pk_fma_f32 v[20:21], s[44:45], v[44:45], v[20:21] op_sel:[1,0,0]
	v_pk_fma_f32 v[22:23], s[52:53], v[44:45], v[22:23] op_sel:[1,0,0]
	v_pk_fma_f32 v[24:25], s[60:61], v[44:45], v[24:25] op_sel:[1,0,0]
	v_pk_fma_f32 v[18:19], s[38:39], v[46:47], v[18:19] op_sel_hi:[0,1,1]
	v_pk_fma_f32 v[20:21], s[46:47], v[46:47], v[20:21] op_sel_hi:[0,1,1]
	v_pk_fma_f32 v[22:23], s[54:55], v[46:47], v[22:23] op_sel_hi:[0,1,1]
	v_pk_fma_f32 v[24:25], s[62:63], v[46:47], v[24:25] op_sel_hi:[0,1,1]
	v_pk_fma_f32 v[18:19], s[38:39], v[48:49], v[18:19] op_sel:[1,0,0]
	v_pk_fma_f32 v[20:21], s[46:47], v[48:49], v[20:21] op_sel:[1,0,0]
	v_pk_fma_f32 v[22:23], s[54:55], v[48:49], v[22:23] op_sel:[1,0,0]
	v_pk_fma_f32 v[24:25], s[62:63], v[48:49], v[24:25] op_sel:[1,0,0]
	s_waitcnt lgkmcnt(0)
	s_load_dwordx8 s[32:39], s[20:21], 0x1800
	s_load_dwordx8 s[40:47], s[20:21], 0x1a00
	s_load_dwordx8 s[48:55], s[20:21], 0x1c00
	s_load_dwordx8 s[56:63], s[20:21], 0x1e00
	v_pk_fma_f32 v[18:19], s[64:65], v[50:51], v[18:19] op_sel_hi:[0,1,1]
	v_pk_fma_f32 v[20:21], s[72:73], v[50:51], v[20:21] op_sel_hi:[0,1,1]
	v_pk_fma_f32 v[22:23], s[80:81], v[50:51], v[22:23] op_sel_hi:[0,1,1]
	v_pk_fma_f32 v[24:25], s[88:89], v[50:51], v[24:25] op_sel_hi:[0,1,1]
	v_pk_fma_f32 v[18:19], s[64:65], v[52:53], v[18:19] op_sel:[1,0,0]
	v_pk_fma_f32 v[20:21], s[72:73], v[52:53], v[20:21] op_sel:[1,0,0]
	v_pk_fma_f32 v[22:23], s[80:81], v[52:53], v[22:23] op_sel:[1,0,0]
	v_pk_fma_f32 v[24:25], s[88:89], v[52:53], v[24:25] op_sel:[1,0,0]
	v_pk_fma_f32 v[18:19], s[66:67], v[54:55], v[18:19] op_sel_hi:[0,1,1]
	v_pk_fma_f32 v[20:21], s[74:75], v[54:55], v[20:21] op_sel_hi:[0,1,1]
	v_pk_fma_f32 v[22:23], s[82:83], v[54:55], v[22:23] op_sel_hi:[0,1,1]
	v_pk_fma_f32 v[24:25], s[90:91], v[54:55], v[24:25] op_sel_hi:[0,1,1]
	v_pk_fma_f32 v[18:19], s[66:67], v[56:57], v[18:19] op_sel:[1,0,0]
	v_pk_fma_f32 v[20:21], s[74:75], v[56:57], v[20:21] op_sel:[1,0,0]
	v_pk_fma_f32 v[22:23], s[82:83], v[56:57], v[22:23] op_sel:[1,0,0]
	v_pk_fma_f32 v[24:25], s[90:91], v[56:57], v[24:25] op_sel:[1,0,0]
	v_pk_fma_f32 v[18:19], s[68:69], v[58:59], v[18:19] op_sel_hi:[0,1,1]
	v_pk_fma_f32 v[20:21], s[76:77], v[58:59], v[20:21] op_sel_hi:[0,1,1]
	v_pk_fma_f32 v[22:23], s[84:85], v[58:59], v[22:23] op_sel_hi:[0,1,1]
	v_pk_fma_f32 v[24:25], s[92:93], v[58:59], v[24:25] op_sel_hi:[0,1,1]
	v_pk_fma_f32 v[18:19], s[68:69], v[60:61], v[18:19] op_sel:[1,0,0]
	v_pk_fma_f32 v[20:21], s[76:77], v[60:61], v[20:21] op_sel:[1,0,0]
	v_pk_fma_f32 v[22:23], s[84:85], v[60:61], v[22:23] op_sel:[1,0,0]
	v_pk_fma_f32 v[24:25], s[92:93], v[60:61], v[24:25] op_sel:[1,0,0]
	v_pk_fma_f32 v[18:19], s[70:71], v[62:63], v[18:19] op_sel_hi:[0,1,1]
	v_pk_fma_f32 v[20:21], s[78:79], v[62:63], v[20:21] op_sel_hi:[0,1,1]
	v_pk_fma_f32 v[22:23], s[86:87], v[62:63], v[22:23] op_sel_hi:[0,1,1]
	v_pk_fma_f32 v[24:25], s[94:95], v[62:63], v[24:25] op_sel_hi:[0,1,1]
	v_pk_fma_f32 v[18:19], s[70:71], v[64:65], v[18:19] op_sel:[1,0,0]
	v_pk_fma_f32 v[20:21], s[78:79], v[64:65], v[20:21] op_sel:[1,0,0]
	v_pk_fma_f32 v[22:23], s[86:87], v[64:65], v[22:23] op_sel:[1,0,0]
	v_pk_fma_f32 v[24:25], s[94:95], v[64:65], v[24:25] op_sel:[1,0,0]
	s_waitcnt lgkmcnt(0)
	s_load_dwordx8 s[64:71], s[20:21], 0x1820
	s_load_dwordx8 s[72:79], s[20:21], 0x1a20
	s_load_dwordx8 s[80:87], s[20:21], 0x1c20
	s_load_dwordx8 s[88:95], s[20:21], 0x1e20
	v_pk_fma_f32 v[26:27], s[32:33], v[34:35], v[26:27] op_sel_hi:[0,1,1]
	v_pk_fma_f32 v[28:29], s[40:41], v[34:35], v[28:29] op_sel_hi:[0,1,1]
	v_pk_fma_f32 v[30:31], s[48:49], v[34:35], v[30:31] op_sel_hi:[0,1,1]
	v_pk_fma_f32 v[32:33], s[56:57], v[34:35], v[32:33] op_sel_hi:[0,1,1]
	v_pk_fma_f32 v[26:27], s[32:33], v[36:37], v[26:27] op_sel:[1,0,0]
	v_pk_fma_f32 v[28:29], s[40:41], v[36:37], v[28:29] op_sel:[1,0,0]
	v_pk_fma_f32 v[30:31], s[48:49], v[36:37], v[30:31] op_sel:[1,0,0]
	v_pk_fma_f32 v[32:33], s[56:57], v[36:37], v[32:33] op_sel:[1,0,0]
	v_pk_fma_f32 v[26:27], s[34:35], v[38:39], v[26:27] op_sel_hi:[0,1,1]
	v_pk_fma_f32 v[28:29], s[42:43], v[38:39], v[28:29] op_sel_hi:[0,1,1]
	v_pk_fma_f32 v[30:31], s[50:51], v[38:39], v[30:31] op_sel_hi:[0,1,1]
	v_pk_fma_f32 v[32:33], s[58:59], v[38:39], v[32:33] op_sel_hi:[0,1,1]
	v_pk_fma_f32 v[26:27], s[34:35], v[40:41], v[26:27] op_sel:[1,0,0]
	v_pk_fma_f32 v[28:29], s[42:43], v[40:41], v[28:29] op_sel:[1,0,0]
	v_pk_fma_f32 v[30:31], s[50:51], v[40:41], v[30:31] op_sel:[1,0,0]
	v_pk_fma_f32 v[32:33], s[58:59], v[40:41], v[32:33] op_sel:[1,0,0]
	v_pk_fma_f32 v[26:27], s[36:37], v[42:43], v[26:27] op_sel_hi:[0,1,1]
	v_pk_fma_f32 v[28:29], s[44:45], v[42:43], v[28:29] op_sel_hi:[0,1,1]
	v_pk_fma_f32 v[30:31], s[52:53], v[42:43], v[30:31] op_sel_hi:[0,1,1]
	v_pk_fma_f32 v[32:33], s[60:61], v[42:43], v[32:33] op_sel_hi:[0,1,1]
	v_pk_fma_f32 v[26:27], s[36:37], v[44:45], v[26:27] op_sel:[1,0,0]
	v_pk_fma_f32 v[28:29], s[44:45], v[44:45], v[28:29] op_sel:[1,0,0]
	v_pk_fma_f32 v[30:31], s[52:53], v[44:45], v[30:31] op_sel:[1,0,0]
	v_pk_fma_f32 v[32:33], s[60:61], v[44:45], v[32:33] op_sel:[1,0,0]
	v_pk_fma_f32 v[26:27], s[38:39], v[46:47], v[26:27] op_sel_hi:[0,1,1]
	v_pk_fma_f32 v[28:29], s[46:47], v[46:47], v[28:29] op_sel_hi:[0,1,1]
	v_pk_fma_f32 v[30:31], s[54:55], v[46:47], v[30:31] op_sel_hi:[0,1,1]
	v_pk_fma_f32 v[32:33], s[62:63], v[46:47], v[32:33] op_sel_hi:[0,1,1]
	v_pk_fma_f32 v[26:27], s[38:39], v[48:49], v[26:27] op_sel:[1,0,0]
	v_pk_fma_f32 v[28:29], s[46:47], v[48:49], v[28:29] op_sel:[1,0,0]
	v_pk_fma_f32 v[30:31], s[54:55], v[48:49], v[30:31] op_sel:[1,0,0]
	v_pk_fma_f32 v[32:33], s[62:63], v[48:49], v[32:33] op_sel:[1,0,0]
	s_waitcnt lgkmcnt(0)
	v_pk_fma_f32 v[26:27], s[64:65], v[50:51], v[26:27] op_sel_hi:[0,1,1]
	v_pk_fma_f32 v[28:29], s[72:73], v[50:51], v[28:29] op_sel_hi:[0,1,1]
	v_pk_fma_f32 v[30:31], s[80:81], v[50:51], v[30:31] op_sel_hi:[0,1,1]
	v_pk_fma_f32 v[32:33], s[88:89], v[50:51], v[32:33] op_sel_hi:[0,1,1]
	v_pk_fma_f32 v[26:27], s[64:65], v[52:53], v[26:27] op_sel:[1,0,0]
	v_pk_fma_f32 v[28:29], s[72:73], v[52:53], v[28:29] op_sel:[1,0,0]
	v_pk_fma_f32 v[30:31], s[80:81], v[52:53], v[30:31] op_sel:[1,0,0]
	v_pk_fma_f32 v[32:33], s[88:89], v[52:53], v[32:33] op_sel:[1,0,0]
	v_pk_fma_f32 v[26:27], s[66:67], v[54:55], v[26:27] op_sel_hi:[0,1,1]
	v_pk_fma_f32 v[28:29], s[74:75], v[54:55], v[28:29] op_sel_hi:[0,1,1]
	v_pk_fma_f32 v[30:31], s[82:83], v[54:55], v[30:31] op_sel_hi:[0,1,1]
	v_pk_fma_f32 v[32:33], s[90:91], v[54:55], v[32:33] op_sel_hi:[0,1,1]
	v_pk_fma_f32 v[26:27], s[66:67], v[56:57], v[26:27] op_sel:[1,0,0]
	v_pk_fma_f32 v[28:29], s[74:75], v[56:57], v[28:29] op_sel:[1,0,0]
	v_pk_fma_f32 v[30:31], s[82:83], v[56:57], v[30:31] op_sel:[1,0,0]
	v_pk_fma_f32 v[32:33], s[90:91], v[56:57], v[32:33] op_sel:[1,0,0]
	v_pk_fma_f32 v[26:27], s[68:69], v[58:59], v[26:27] op_sel_hi:[0,1,1]
	v_pk_fma_f32 v[28:29], s[76:77], v[58:59], v[28:29] op_sel_hi:[0,1,1]
	v_pk_fma_f32 v[30:31], s[84:85], v[58:59], v[30:31] op_sel_hi:[0,1,1]
	v_pk_fma_f32 v[32:33], s[92:93], v[58:59], v[32:33] op_sel_hi:[0,1,1]
	v_pk_fma_f32 v[26:27], s[68:69], v[60:61], v[26:27] op_sel:[1,0,0]
	v_pk_fma_f32 v[28:29], s[76:77], v[60:61], v[28:29] op_sel:[1,0,0]
	v_pk_fma_f32 v[30:31], s[84:85], v[60:61], v[30:31] op_sel:[1,0,0]
	v_pk_fma_f32 v[32:33], s[92:93], v[60:61], v[32:33] op_sel:[1,0,0]
	v_pk_fma_f32 v[26:27], s[70:71], v[62:63], v[26:27] op_sel_hi:[0,1,1]
	v_pk_fma_f32 v[28:29], s[78:79], v[62:63], v[28:29] op_sel_hi:[0,1,1]
	v_pk_fma_f32 v[30:31], s[86:87], v[62:63], v[30:31] op_sel_hi:[0,1,1]
	v_pk_fma_f32 v[32:33], s[94:95], v[62:63], v[32:33] op_sel_hi:[0,1,1]
	v_pk_fma_f32 v[26:27], s[70:71], v[64:65], v[26:27] op_sel:[1,0,0]
	v_pk_fma_f32 v[28:29], s[78:79], v[64:65], v[28:29] op_sel:[1,0,0]
	v_pk_fma_f32 v[30:31], s[86:87], v[64:65], v[30:31] op_sel:[1,0,0]
	v_pk_fma_f32 v[32:33], s[94:95], v[64:65], v[32:33] op_sel:[1,0,0]
	s_lshl_b32 s9, s23, 13
	v_add_u32_e32 v98, s9, v100
	ds_write_b64 v98, v[2:3] offset:0
	ds_write_b64 v98, v[4:5] offset:512
	ds_write_b64 v98, v[6:7] offset:1024
	ds_write_b64 v98, v[8:9] offset:1536
	ds_write_b64 v98, v[10:11] offset:2048
	ds_write_b64 v98, v[12:13] offset:2560
	ds_write_b64 v98, v[14:15] offset:3072
	ds_write_b64 v98, v[16:17] offset:3584
	ds_write_b64 v98, v[18:19] offset:4096
	ds_write_b64 v98, v[20:21] offset:4608
	ds_write_b64 v98, v[22:23] offset:5120
	ds_write_b64 v98, v[24:25] offset:5632
	ds_write_b64 v98, v[26:27] offset:6144
	ds_write_b64 v98, v[28:29] offset:6656
	ds_write_b64 v98, v[30:31] offset:7168
	ds_write_b64 v98, v[32:33] offset:7680
	s_lshl_b32 s9, s23, 10
	v_add_u32_e32 v99, s9, v100
	s_waitcnt lgkmcnt(0)
	s_barrier
	ds_read_b64 v[34:35], v99 offset:0
	ds_read_b64 v[36:37], v99 offset:8192
	ds_read_b64 v[38:39], v99 offset:16384
	ds_read_b64 v[40:41], v99 offset:24576
	ds_read_b64 v[42:43], v99 offset:32768
	ds_read_b64 v[44:45], v99 offset:40960
	ds_read_b64 v[46:47], v99 offset:49152
	ds_read_b64 v[48:49], v99 offset:57344
	ds_read_b64 v[50:51], v99 offset:512
	ds_read_b64 v[52:53], v99 offset:8704
	ds_read_b64 v[54:55], v99 offset:16896
	ds_read_b64 v[56:57], v99 offset:25088
	ds_read_b64 v[58:59], v99 offset:33280
	ds_read_b64 v[60:61], v99 offset:41472
	ds_read_b64 v[62:63], v99 offset:49664
	ds_read_b64 v[64:65], v99 offset:57856
	s_lshl_b32 s8, s27, 4
	s_lshl_b32 s9, s23, 1
	s_add_u32 s8, s8, s9
	s_lshl_b32 s8, s8, 11
	s_lshl_b32 s9, s30, 9
	s_add_u32 s8, s8, s9
	s_add_u32 s28, s28, s8
	s_addc_u32 s29, s29, 0
	s_waitcnt lgkmcnt(14)
	v_pk_add_f32 v[34:35], v[34:35], v[36:37]
	s_waitcnt lgkmcnt(13)
	v_pk_add_f32 v[34:35], v[34:35], v[38:39]
	s_waitcnt lgkmcnt(12)
	v_pk_add_f32 v[34:35], v[34:35], v[40:41]
	s_waitcnt lgkmcnt(11)
	v_pk_add_f32 v[34:35], v[34:35], v[42:43]
	s_waitcnt lgkmcnt(10)
	v_pk_add_f32 v[34:35], v[34:35], v[44:45]
	s_waitcnt lgkmcnt(9)
	v_pk_add_f32 v[34:35], v[34:35], v[46:47]
	s_waitcnt lgkmcnt(8)
	v_pk_add_f32 v[34:35], v[34:35], v[48:49]
	global_store_dwordx2 v100, v[34:35], s[28:29]
	s_waitcnt lgkmcnt(6)
	v_pk_add_f32 v[50:51], v[50:51], v[52:53]
	s_waitcnt lgkmcnt(5)
	v_pk_add_f32 v[50:51], v[50:51], v[54:55]
	s_waitcnt lgkmcnt(4)
	v_pk_add_f32 v[50:51], v[50:51], v[56:57]
	s_waitcnt lgkmcnt(3)
	v_pk_add_f32 v[50:51], v[50:51], v[58:59]
	s_waitcnt lgkmcnt(2)
	v_pk_add_f32 v[50:51], v[50:51], v[60:61]
	s_waitcnt lgkmcnt(1)
	v_pk_add_f32 v[50:51], v[50:51], v[62:63]
	s_waitcnt lgkmcnt(0)
	v_pk_add_f32 v[50:51], v[50:51], v[64:65]
	global_store_dwordx2 v100, v[50:51], s[28:29] offset:2048
